# speedup vs baseline: 1.0029x; 1.0029x over previous
.LBB1_2:
	v_add_u32_e32 v186, s21, v216
	ds_read_b64_tr_b16 v[122:123], v186 offset:24576
	ds_read_b64_tr_b16 v[124:125], v186 offset:25088
	s_waitcnt lgkmcnt(9)
	v_mfma_f32_32x32x16_f16 v[98:113], v[82:85], v[174:177], v[34:49]
	v_add_f32_e32 v86, v66, v67
	v_add_f32_e32 v86, v68, v86
	v_add_f32_e32 v86, v69, v86
	v_add_f32_e32 v86, v70, v86
	v_add_f32_e32 v86, v71, v86
	v_cvt_pkrtz_f16_f32 v158, v66, v67
	v_cvt_pkrtz_f16_f32 v159, v68, v69
	ds_read_b64_tr_b16 v[118:119], v186 offset:28672
	ds_read_b64_tr_b16 v[120:121], v186 offset:29184
	v_add_f32_e32 v66, v72, v86
	s_waitcnt lgkmcnt(10)
	v_mfma_f32_32x32x16_f16 v[82:97], v[182:185], v[174:177], v[34:49]
	v_add_f32_e32 v66, v73, v66
	v_add_f32_e32 v66, v74, v66
	v_add_f32_e32 v66, v75, v66
	v_cvt_pkrtz_f16_f32 v160, v70, v71
	v_cvt_pkrtz_f16_f32 v161, v72, v73
	ds_read_b64_tr_b16 v[114:115], v186 offset:25600
	ds_read_b64_tr_b16 v[116:117], v186 offset:26112
	s_waitcnt lgkmcnt(11)
	v_mfma_f32_32x32x16_f16 v[98:113], v[178:181], v[170:173], v[98:113]
	v_add_f32_e32 v66, v76, v66
	v_add_f32_e32 v66, v77, v66
	v_add_f32_e32 v66, v78, v66
	v_add_f32_e32 v66, v79, v66
	v_cvt_pkrtz_f16_f32 v154, v74, v75
	v_cvt_pkrtz_f16_f32 v155, v76, v77
	ds_read_b64_tr_b16 v[74:75], v186 offset:29696
	ds_read_b64_tr_b16 v[76:77], v186 offset:30208
	s_waitcnt lgkmcnt(12)
	v_mfma_f32_32x32x16_f16 v[82:97], v[142:145], v[170:173], v[82:97]
	v_add_f32_e32 v66, v80, v66
	v_add_f32_e32 v66, v81, v66
	v_add_f32_e32 v66, v50, v66
	v_add_f32_e32 v66, v51, v66
	v_cvt_pkrtz_f16_f32 v156, v78, v79
	v_cvt_pkrtz_f16_f32 v157, v80, v81
	ds_read_b64_tr_b16 v[70:71], v186 offset:26624
	ds_read_b64_tr_b16 v[72:73], v186 offset:27136
	s_waitcnt lgkmcnt(13)
	v_mfma_f32_32x32x16_f16 v[98:113], v[138:141], v[166:169], v[98:113]
	v_add_f32_e32 v66, v52, v66
	v_add_f32_e32 v66, v53, v66
	v_add_f32_e32 v66, v54, v66
	v_add_f32_e32 v78, v55, v66
	v_cvt_pkrtz_f16_f32 v150, v50, v51
	v_cvt_pkrtz_f16_f32 v151, v52, v53
	ds_read_b64_tr_b16 v[66:67], v186 offset:30720
	ds_read_b64_tr_b16 v[68:69], v186 offset:31232
	s_waitcnt lgkmcnt(14)
	v_mfma_f32_32x32x16_f16 v[82:97], v[134:137], v[166:169], v[82:97]
	v_add_f32_e32 v50, v56, v78
	v_add_f32_e32 v50, v57, v50
	v_add_f32_e32 v50, v58, v50
	v_add_f32_e32 v50, v59, v50
	v_cvt_pkrtz_f16_f32 v152, v54, v55
	v_cvt_pkrtz_f16_f32 v153, v56, v57
	ds_read_b64_tr_b16 v[54:55], v186 offset:27648
	ds_read_b64_tr_b16 v[56:57], v186 offset:28160
	s_waitcnt lgkmcnt(14)
	v_mfma_f32_32x32x16_f16 v[98:113], v[130:133], v[162:165], v[98:113]
	v_add_f32_e32 v50, v60, v50
	v_add_f32_e32 v50, v61, v50
	v_add_f32_e32 v50, v62, v50
	v_add_f32_e32 v78, v63, v50
	v_cvt_pkrtz_f16_f32 v146, v58, v59
	v_cvt_pkrtz_f16_f32 v147, v60, v61
	ds_read_b64_tr_b16 v[50:51], v186 offset:31744
	ds_read_b64_tr_b16 v[52:53], v186 offset:32256
	v_mfma_f32_32x32x16_f16 v[82:97], v[126:129], v[162:165], v[82:97]
	v_add_f32_e32 v58, v64, v78
	v_add_f32_e32 v58, v65, v58
	v_add_f32_e32 v58, 0, v58
	v_cvt_pkrtz_f16_f32 v148, v62, v63
	v_cvt_pkrtz_f16_f32 v149, v64, v65
	s_nop 0
	v_add_f32_e32 v201, v201, v58
	v_max_f32_e32 v58, v99, v99
	v_max_f32_e32 v59, v98, v98
	v_max_f32_e32 v58, v59, v58
	s_nop 1
	v_max3_f32 v59, v100, v101, v83
	v_max3_f32 v58, v58, v82, v84
	v_max3_f32 v58, v58, v85, v102
	v_max3_f32 v59, v59, v104, v105
	v_max3_f32 v58, v58, v103, v86
	v_max3_f32 v59, v59, v88, v89
	v_max3_f32 v58, v58, v87, v106
	v_max3_f32 v59, v59, v108, v109
	v_max3_f32 v58, v58, v107, v90
	v_max3_f32 v59, v59, v92, v93
	v_max3_f32 v58, v58, v91, v110
	v_max3_f32 v59, v59, v112, v113
	v_max3_f32 v58, v58, v111, v94
	v_max3_f32 v59, v59, v96, v97
	v_max3_f32 v58, v58, v95, v59
	v_mov_b32_e32 v59, v58
	s_nop 1
	v_permlane32_swap_b32_e32 v58, v59
	v_max_f32_e32 v58, v58, v59
	v_cmp_lt_f32_e32 vcc, s34, v58
	s_cmp_lg_u64 vcc, 0
	s_cselect_b64 s[20:21], -1, 0
	s_cbranch_vccnz .LBB1_14
	v_mov_b32_e32 v220, v219

.LBB1_6:
	v_add_u32_e32 v50, s35, v216
	ds_read_b64_tr_b16 v[190:191], v50 offset:24576
	ds_read_b64_tr_b16 v[192:193], v50 offset:25088
	s_waitcnt lgkmcnt(9)
	v_mfma_f32_32x32x16_f16 v[130:145], v[118:121], v[174:177], v[34:49]
	v_add_f32_e32 v51, v98, v99
	v_add_f32_e32 v51, v100, v51
	v_add_f32_e32 v51, v101, v51
	v_add_f32_e32 v51, v102, v51
	v_add_f32_e32 v51, v103, v51
	v_cvt_pkrtz_f16_f32 v158, v98, v99
	v_cvt_pkrtz_f16_f32 v159, v100, v101
	ds_read_b64_tr_b16 v[182:183], v50 offset:28672
	ds_read_b64_tr_b16 v[184:185], v50 offset:29184
	s_waitcnt lgkmcnt(10)
	v_mfma_f32_32x32x16_f16 v[114:129], v[178:181], v[174:177], v[34:49]
	v_add_f32_e32 v51, v104, v51
	v_add_f32_e32 v51, v105, v51
	v_add_f32_e32 v51, v106, v51
	v_add_f32_e32 v51, v107, v51
	v_cvt_pkrtz_f16_f32 v160, v102, v103
	v_cvt_pkrtz_f16_f32 v161, v104, v105
	ds_read_b64_tr_b16 v[178:179], v50 offset:25600
	ds_read_b64_tr_b16 v[180:181], v50 offset:26112
	s_waitcnt lgkmcnt(11)
	v_mfma_f32_32x32x16_f16 v[130:145], v[186:189], v[170:173], v[130:145]
	v_add_f32_e32 v51, v108, v51
	v_add_f32_e32 v51, v109, v51
	v_add_f32_e32 v51, v110, v51
	v_add_f32_e32 v51, v111, v51
	v_cvt_pkrtz_f16_f32 v154, v106, v107
	v_cvt_pkrtz_f16_f32 v155, v108, v109
	ds_read_b64_tr_b16 v[186:187], v50 offset:29696
	ds_read_b64_tr_b16 v[188:189], v50 offset:30208
	s_waitcnt lgkmcnt(12)
	v_mfma_f32_32x32x16_f16 v[114:129], v[78:81], v[170:173], v[114:129]
	v_add_f32_e32 v51, v112, v51
	v_add_f32_e32 v51, v113, v51
	v_add_f32_e32 v51, v82, v51
	v_add_f32_e32 v51, v83, v51
	v_cvt_pkrtz_f16_f32 v156, v110, v111
	v_cvt_pkrtz_f16_f32 v157, v112, v113
	ds_read_b64_tr_b16 v[110:111], v50 offset:26624
	ds_read_b64_tr_b16 v[112:113], v50 offset:27136
	s_waitcnt lgkmcnt(13)
	v_mfma_f32_32x32x16_f16 v[130:145], v[74:77], v[166:169], v[130:145]
	v_add_f32_e32 v51, v84, v51
	v_add_f32_e32 v51, v85, v51
	v_add_f32_e32 v51, v86, v51
	v_add_f32_e32 v51, v87, v51
	v_cvt_pkrtz_f16_f32 v150, v82, v83
	v_cvt_pkrtz_f16_f32 v151, v84, v85
	ds_read_b64_tr_b16 v[106:107], v50 offset:30720
	ds_read_b64_tr_b16 v[108:109], v50 offset:31232
	s_waitcnt lgkmcnt(14)
	v_mfma_f32_32x32x16_f16 v[114:129], v[62:65], v[166:169], v[114:129]
	v_add_f32_e32 v51, v88, v51
	v_add_f32_e32 v51, v89, v51
	v_add_f32_e32 v51, v90, v51
	v_add_f32_e32 v51, v91, v51
	v_cvt_pkrtz_f16_f32 v152, v86, v87
	v_cvt_pkrtz_f16_f32 v153, v88, v89
	ds_read_b64_tr_b16 v[102:103], v50 offset:27648
	ds_read_b64_tr_b16 v[104:105], v50 offset:28160
	s_waitcnt lgkmcnt(14)
	v_mfma_f32_32x32x16_f16 v[130:145], v[70:73], v[162:165], v[130:145]
	v_add_f32_e32 v51, v92, v51
	v_add_f32_e32 v51, v93, v51
	v_add_f32_e32 v51, v94, v51
	v_add_f32_e32 v51, v95, v51
	v_cvt_pkrtz_f16_f32 v146, v90, v91
	v_cvt_pkrtz_f16_f32 v147, v92, v93
	ds_read_b64_tr_b16 v[98:99], v50 offset:31744
	ds_read_b64_tr_b16 v[100:101], v50 offset:32256
	v_mfma_f32_32x32x16_f16 v[114:129], v[58:61], v[162:165], v[114:129]
	v_add_f32_e32 v50, v96, v51
	v_add_f32_e32 v50, v97, v50
	v_add_f32_e32 v50, 0, v50
	v_cvt_pkrtz_f16_f32 v148, v94, v95
	v_cvt_pkrtz_f16_f32 v149, v96, v97
	s_nop 0
	v_add_f32_e32 v51, v201, v50
	v_max_f32_e32 v50, v131, v131
	v_max_f32_e32 v52, v130, v130
	v_max_f32_e32 v50, v52, v50
	s_nop 1
	v_max3_f32 v52, v132, v133, v115
	v_max3_f32 v50, v50, v114, v116
	v_max3_f32 v50, v50, v117, v134
	v_max3_f32 v52, v52, v136, v137
	v_max3_f32 v50, v50, v135, v118
	v_max3_f32 v52, v52, v120, v121
	v_max3_f32 v50, v50, v119, v138
	v_max3_f32 v52, v52, v140, v141
	v_max3_f32 v50, v50, v139, v122
	v_max3_f32 v52, v52, v124, v125
	v_max3_f32 v50, v50, v123, v142
	v_max3_f32 v52, v52, v144, v145
	v_max3_f32 v50, v50, v143, v126
	v_max3_f32 v52, v52, v128, v129
	v_max3_f32 v50, v50, v127, v52
	v_mov_b32_e32 v52, v50
	s_nop 1
	v_permlane32_swap_b32_e32 v50, v52
	v_max_f32_e32 v50, v50, v52
	v_cmp_lt_f32_e32 vcc, s34, v50
	s_cmp_lg_u64 vcc, 0
	s_cselect_b64 s[20:21], -1, 0
	s_cbranch_vccnz .LBB1_17
	v_mov_b32_e32 v201, v51
	v_mov_b32_e32 v219, v220

.LBB1_20:
	ds_read_b64_tr_b16 v[190:191], v216 offset:40960
	ds_read_b64_tr_b16 v[192:193], v216 offset:41472
	s_waitcnt lgkmcnt(9)
	v_mfma_f32_32x32x16_f16 v[110:125], v[82:85], v[174:177], v[34:49]
	v_add_f32_e32 v86, v66, v67
	v_add_f32_e32 v86, v68, v86
	v_add_f32_e32 v86, v69, v86
	v_add_f32_e32 v86, v70, v86
	v_add_f32_e32 v86, v71, v86
	v_cvt_pkrtz_f16_f32 v158, v66, v67
	v_cvt_pkrtz_f16_f32 v159, v68, v69
	ds_read_b64_tr_b16 v[186:187], v216 offset:45056
	ds_read_b64_tr_b16 v[188:189], v216 offset:45568
	v_add_f32_e32 v66, v72, v86
	s_waitcnt lgkmcnt(10)
	v_mfma_f32_32x32x16_f16 v[82:97], v[182:185], v[174:177], v[34:49]
	v_add_f32_e32 v66, v73, v66
	v_add_f32_e32 v66, v74, v66
	v_add_f32_e32 v66, v75, v66
	v_cvt_pkrtz_f16_f32 v160, v70, v71
	v_cvt_pkrtz_f16_f32 v161, v72, v73
	ds_read_b64_tr_b16 v[182:183], v216 offset:41984
	ds_read_b64_tr_b16 v[184:185], v216 offset:42496
	s_waitcnt lgkmcnt(11)
	v_mfma_f32_32x32x16_f16 v[110:125], v[178:181], v[170:173], v[110:125]
	v_add_f32_e32 v66, v76, v66
	v_add_f32_e32 v66, v77, v66
	v_add_f32_e32 v66, v78, v66
	v_add_f32_e32 v66, v79, v66
	v_cvt_pkrtz_f16_f32 v154, v74, v75
	v_cvt_pkrtz_f16_f32 v155, v76, v77
	ds_read_b64_tr_b16 v[178:179], v216 offset:46080
	ds_read_b64_tr_b16 v[180:181], v216 offset:46592
	s_waitcnt lgkmcnt(12)
	v_mfma_f32_32x32x16_f16 v[82:97], v[142:145], v[170:173], v[82:97]
	v_add_f32_e32 v66, v80, v66
	v_add_f32_e32 v66, v81, v66
	v_add_f32_e32 v66, v50, v66
	v_add_f32_e32 v66, v51, v66
	v_cvt_pkrtz_f16_f32 v156, v78, v79
	v_cvt_pkrtz_f16_f32 v157, v80, v81
	ds_read_b64_tr_b16 v[142:143], v216 offset:43008
	ds_read_b64_tr_b16 v[144:145], v216 offset:43520
	s_waitcnt lgkmcnt(13)
	v_mfma_f32_32x32x16_f16 v[110:125], v[138:141], v[166:169], v[110:125]
	v_add_f32_e32 v66, v52, v66
	v_add_f32_e32 v66, v53, v66
	v_add_f32_e32 v66, v54, v66
	v_add_f32_e32 v66, v55, v66
	v_cvt_pkrtz_f16_f32 v150, v50, v51
	v_cvt_pkrtz_f16_f32 v151, v52, v53
	ds_read_b64_tr_b16 v[138:139], v216 offset:47104
	ds_read_b64_tr_b16 v[140:141], v216 offset:47616
	s_waitcnt lgkmcnt(14)
	v_mfma_f32_32x32x16_f16 v[82:97], v[134:137], v[166:169], v[82:97]
	v_add_f32_e32 v50, v56, v66
	v_add_f32_e32 v50, v57, v50
	v_add_f32_e32 v50, v58, v50
	v_add_f32_e32 v50, v59, v50
	v_cvt_pkrtz_f16_f32 v152, v54, v55
	v_cvt_pkrtz_f16_f32 v153, v56, v57
	ds_read_b64_tr_b16 v[134:135], v216 offset:44032
	ds_read_b64_tr_b16 v[136:137], v216 offset:44544
	s_waitcnt lgkmcnt(14)
	v_mfma_f32_32x32x16_f16 v[110:125], v[130:133], v[162:165], v[110:125]
	v_add_f32_e32 v50, v60, v50
	v_add_f32_e32 v50, v61, v50
	v_add_f32_e32 v50, v62, v50
	v_add_f32_e32 v50, v63, v50
	v_cvt_pkrtz_f16_f32 v146, v58, v59
	v_cvt_pkrtz_f16_f32 v147, v60, v61
	ds_read_b64_tr_b16 v[130:131], v216 offset:48128
	ds_read_b64_tr_b16 v[132:133], v216 offset:48640
	v_mfma_f32_32x32x16_f16 v[82:97], v[126:129], v[162:165], v[82:97]
	v_add_f32_e32 v50, v64, v50
	v_add_f32_e32 v50, v65, v50
	v_add_f32_e32 v50, 0, v50
	v_cvt_pkrtz_f16_f32 v148, v62, v63
	v_cvt_pkrtz_f16_f32 v149, v64, v65
	s_nop 0
	v_add_f32_e32 v67, v201, v50
	v_max_f32_e32 v50, v111, v111
	v_max_f32_e32 v51, v110, v110
	v_max_f32_e32 v50, v51, v50
	s_nop 1
	v_max3_f32 v51, v112, v113, v83
	v_max3_f32 v50, v50, v82, v84
	v_max3_f32 v50, v50, v85, v114
	v_max3_f32 v51, v51, v116, v117
	v_max3_f32 v50, v50, v115, v86
	v_max3_f32 v51, v51, v88, v89
	v_max3_f32 v50, v50, v87, v118
	v_max3_f32 v51, v51, v120, v121
	v_max3_f32 v50, v50, v119, v90
	v_max3_f32 v51, v51, v92, v93
	v_max3_f32 v50, v50, v91, v122
	v_max3_f32 v51, v51, v124, v125
	v_max3_f32 v50, v50, v123, v94
	v_max3_f32 v51, v51, v96, v97
	v_max3_f32 v50, v50, v95, v51
	v_mov_b32_e32 v51, v50
	s_nop 1
	v_permlane32_swap_b32_e32 v50, v51
	v_max_f32_e32 v50, v50, v51
	s_mov_b32 s6, 0x41000000
	v_cmp_lt_f32_e32 vcc, s6, v50
	s_cmp_lg_u64 vcc, 0
	s_cselect_b64 s[6:7], -1, 0
	s_cbranch_vccnz .LBB1_80
	s_mov_b64 s[8:9], -1
	v_mov_b32_e32 v66, v35

.LBB1_26:
	ds_read_b64_tr_b16 v[186:187], v216 offset:24576
	ds_read_b64_tr_b16 v[188:189], v216 offset:25088
	s_waitcnt lgkmcnt(9)
	v_mfma_f32_32x32x16_f16 v[110:125], v[86:89], v[174:177], v[50:65]
	v_add_f32_e32 v82, v94, v95
	v_add_f32_e32 v82, v96, v82
	v_add_f32_e32 v82, v97, v82
	v_add_f32_e32 v82, v98, v82
	v_add_f32_e32 v82, v99, v82
	v_cvt_pkrtz_f16_f32 v158, v94, v95
	v_cvt_pkrtz_f16_f32 v159, v96, v97
	ds_read_b64_tr_b16 v[182:183], v216 offset:28672
	ds_read_b64_tr_b16 v[184:185], v216 offset:29184
	v_add_f32_e32 v82, v100, v82
	v_add_f32_e32 v82, v101, v82
	v_add_f32_e32 v82, v102, v82
	v_add_f32_e32 v130, v103, v82
	s_waitcnt lgkmcnt(10)
	v_mfma_f32_32x32x16_f16 v[82:97], v[126:129], v[174:177], v[50:65]
	v_cvt_pkrtz_f16_f32 v160, v98, v99
	v_cvt_pkrtz_f16_f32 v161, v100, v101
	ds_read_b64_tr_b16 v[178:179], v216 offset:25600
	ds_read_b64_tr_b16 v[180:181], v216 offset:26112
	s_waitcnt lgkmcnt(11)
	v_mfma_f32_32x32x16_f16 v[110:125], v[194:197], v[170:173], v[110:125]
	v_add_f32_e32 v98, v104, v130
	v_add_f32_e32 v98, v105, v98
	v_add_f32_e32 v98, v106, v98
	v_add_f32_e32 v98, v107, v98
	v_cvt_pkrtz_f16_f32 v154, v102, v103
	v_cvt_pkrtz_f16_f32 v155, v104, v105
	ds_read_b64_tr_b16 v[142:143], v216 offset:29696
	ds_read_b64_tr_b16 v[144:145], v216 offset:30208
	s_waitcnt lgkmcnt(12)
	v_mfma_f32_32x32x16_f16 v[82:97], v[42:45], v[170:173], v[82:97]
	v_add_f32_e32 v98, v108, v98
	v_add_f32_e32 v98, v109, v98
	v_add_f32_e32 v98, v66, v98
	v_add_f32_e32 v98, v67, v98
	v_cvt_pkrtz_f16_f32 v156, v106, v107
	v_cvt_pkrtz_f16_f32 v157, v108, v109
	ds_read_b64_tr_b16 v[138:139], v216 offset:26624
	ds_read_b64_tr_b16 v[140:141], v216 offset:27136
	s_waitcnt lgkmcnt(13)
	v_mfma_f32_32x32x16_f16 v[110:125], v[190:193], v[166:169], v[110:125]
	v_add_f32_e32 v42, v68, v98
	v_add_f32_e32 v42, v69, v42
	v_add_f32_e32 v42, v70, v42
	v_add_f32_e32 v42, v71, v42
	v_cvt_pkrtz_f16_f32 v150, v66, v67
	v_cvt_pkrtz_f16_f32 v151, v68, v69
	ds_read_b64_tr_b16 v[134:135], v216 offset:30720
	ds_read_b64_tr_b16 v[136:137], v216 offset:31232
	s_waitcnt lgkmcnt(14)
	v_mfma_f32_32x32x16_f16 v[82:97], v[38:41], v[166:169], v[82:97]
	v_add_f32_e32 v42, v72, v42
	v_add_f32_e32 v42, v73, v42
	v_add_f32_e32 v42, v74, v42
	v_add_f32_e32 v42, v75, v42
	v_cvt_pkrtz_f16_f32 v152, v70, v71
	v_cvt_pkrtz_f16_f32 v153, v72, v73
	ds_read_b64_tr_b16 v[130:131], v216 offset:27648
	ds_read_b64_tr_b16 v[132:133], v216 offset:28160
	s_waitcnt lgkmcnt(14)
	v_mfma_f32_32x32x16_f16 v[110:125], v[46:49], v[162:165], v[110:125]
	v_add_f32_e32 v38, v76, v42
	v_add_f32_e32 v38, v77, v38
	v_add_f32_e32 v38, v78, v38
	v_add_f32_e32 v38, v79, v38
	v_cvt_pkrtz_f16_f32 v146, v74, v75
	v_cvt_pkrtz_f16_f32 v147, v76, v77
	ds_read_b64_tr_b16 v[126:127], v216 offset:31744
	ds_read_b64_tr_b16 v[128:129], v216 offset:32256
	v_mfma_f32_32x32x16_f16 v[82:97], v[34:37], v[162:165], v[82:97]
	v_add_f32_e32 v38, v80, v38
	v_add_f32_e32 v38, v81, v38
	v_add_f32_e32 v38, 0, v38
	v_cvt_pkrtz_f16_f32 v148, v78, v79
	v_cvt_pkrtz_f16_f32 v149, v80, v81
	v_max_f32_e32 v34, v111, v111
	v_max_f32_e32 v35, v110, v110
	v_max_f32_e32 v34, v35, v34
	s_nop 3
	v_max3_f32 v35, v112, v113, v83
	v_max3_f32 v34, v34, v82, v84
	v_max3_f32 v34, v34, v85, v114
	v_max3_f32 v35, v35, v116, v117
	v_max3_f32 v34, v34, v115, v86
	v_max3_f32 v35, v35, v88, v89
	v_max3_f32 v34, v34, v87, v118
	v_max3_f32 v35, v35, v120, v121
	v_max3_f32 v34, v34, v119, v90
	v_max3_f32 v35, v35, v92, v93
	v_max3_f32 v34, v34, v91, v122
	v_max3_f32 v35, v35, v124, v125
	v_max3_f32 v34, v34, v123, v94
	v_max3_f32 v35, v35, v96, v97
	v_max3_f32 v34, v34, v95, v35
	v_mov_b32_e32 v35, v34
	s_nop 1
	v_permlane32_swap_b32_e32 v34, v35
	v_max_f32_e32 v34, v34, v35
	s_mov_b32 s6, 0x41000000
	v_cmp_lt_f32_e32 vcc, s6, v34
	s_cmp_lg_u64 vcc, 0
	v_add_f32_e32 v79, v205, v38
	s_cselect_b64 s[6:7], -1, 0
	s_cbranch_vccnz .LBB1_83
	s_mov_b64 s[8:9], -1
	v_mov_b32_e32 v78, v51

.LBB1_32:
	ds_read_b64_tr_b16 v[186:187], v216 offset:32768
	ds_read_b64_tr_b16 v[188:189], v216 offset:33280
	s_waitcnt lgkmcnt(9)
	v_mfma_f32_32x32x16_f16 v[110:125], v[86:89], v[174:177], v[34:49]
	v_add_f32_e32 v82, v94, v95
	v_add_f32_e32 v82, v96, v82
	v_add_f32_e32 v82, v97, v82
	v_add_f32_e32 v82, v98, v82
	v_add_f32_e32 v82, v99, v82
	v_cvt_pkrtz_f16_f32 v158, v94, v95
	v_cvt_pkrtz_f16_f32 v159, v96, v97
	ds_read_b64_tr_b16 v[182:183], v216 offset:36864
	ds_read_b64_tr_b16 v[184:185], v216 offset:37376
	v_add_f32_e32 v82, v100, v82
	v_add_f32_e32 v82, v101, v82
	v_add_f32_e32 v82, v102, v82
	v_add_f32_e32 v126, v103, v82
	s_waitcnt lgkmcnt(10)
	v_mfma_f32_32x32x16_f16 v[82:97], v[194:197], v[174:177], v[34:49]
	v_cvt_pkrtz_f16_f32 v160, v98, v99
	v_cvt_pkrtz_f16_f32 v161, v100, v101
	ds_read_b64_tr_b16 v[178:179], v216 offset:33792
	ds_read_b64_tr_b16 v[180:181], v216 offset:34304
	s_waitcnt lgkmcnt(11)
	v_mfma_f32_32x32x16_f16 v[110:125], v[198:201], v[170:173], v[110:125]
	v_add_f32_e32 v98, v104, v126
	v_add_f32_e32 v98, v105, v98
	v_add_f32_e32 v98, v106, v98
	v_add_f32_e32 v98, v107, v98
	v_cvt_pkrtz_f16_f32 v154, v102, v103
	v_cvt_pkrtz_f16_f32 v155, v104, v105
	ds_read_b64_tr_b16 v[142:143], v216 offset:37888
	ds_read_b64_tr_b16 v[144:145], v216 offset:38400
	s_waitcnt lgkmcnt(12)
	v_mfma_f32_32x32x16_f16 v[82:97], v[78:81], v[170:173], v[82:97]
	v_add_f32_e32 v98, v108, v98
	v_add_f32_e32 v98, v109, v98
	v_add_f32_e32 v98, v62, v98
	v_add_f32_e32 v98, v63, v98
	v_cvt_pkrtz_f16_f32 v156, v106, v107
	v_cvt_pkrtz_f16_f32 v157, v108, v109
	ds_read_b64_tr_b16 v[138:139], v216 offset:34816
	ds_read_b64_tr_b16 v[140:141], v216 offset:35328
	s_waitcnt lgkmcnt(13)
	v_mfma_f32_32x32x16_f16 v[110:125], v[190:193], v[166:169], v[110:125]
	v_add_f32_e32 v78, v64, v98
	v_add_f32_e32 v78, v65, v78
	v_add_f32_e32 v78, v66, v78
	v_add_f32_e32 v78, v67, v78
	v_cvt_pkrtz_f16_f32 v150, v62, v63
	v_cvt_pkrtz_f16_f32 v151, v64, v65
	ds_read_b64_tr_b16 v[134:135], v216 offset:38912
	ds_read_b64_tr_b16 v[136:137], v216 offset:39424
	s_waitcnt lgkmcnt(14)
	v_mfma_f32_32x32x16_f16 v[82:97], v[54:57], v[166:169], v[82:97]
	v_add_f32_e32 v62, v68, v78
	v_add_f32_e32 v62, v69, v62
	v_add_f32_e32 v62, v70, v62
	v_add_f32_e32 v62, v71, v62
	v_cvt_pkrtz_f16_f32 v152, v66, v67
	v_cvt_pkrtz_f16_f32 v153, v68, v69
	ds_read_b64_tr_b16 v[130:131], v216 offset:35840
	ds_read_b64_tr_b16 v[132:133], v216 offset:36352
	s_waitcnt lgkmcnt(14)
	v_mfma_f32_32x32x16_f16 v[110:125], v[58:61], v[162:165], v[110:125]
	v_add_f32_e32 v54, v72, v62
	v_add_f32_e32 v54, v73, v54
	v_add_f32_e32 v54, v74, v54
	v_add_f32_e32 v54, v75, v54
	v_cvt_pkrtz_f16_f32 v146, v70, v71
	v_cvt_pkrtz_f16_f32 v147, v72, v73
	ds_read_b64_tr_b16 v[126:127], v216 offset:39936
	ds_read_b64_tr_b16 v[128:129], v216 offset:40448
	v_mfma_f32_32x32x16_f16 v[82:97], v[50:53], v[162:165], v[82:97]
	v_add_f32_e32 v54, v76, v54
	v_add_f32_e32 v54, v77, v54
	v_add_f32_e32 v54, 0, v54
	v_cvt_pkrtz_f16_f32 v148, v74, v75
	v_cvt_pkrtz_f16_f32 v149, v76, v77
	v_max_f32_e32 v50, v111, v111
	v_max_f32_e32 v51, v110, v110
	v_max_f32_e32 v50, v51, v50
	s_nop 3
	v_max3_f32 v51, v112, v113, v83
	v_max3_f32 v50, v50, v82, v84
	v_max3_f32 v50, v50, v85, v114
	v_max3_f32 v51, v51, v116, v117
	v_max3_f32 v50, v50, v115, v86
	v_max3_f32 v51, v51, v88, v89
	v_max3_f32 v50, v50, v87, v118
	v_max3_f32 v51, v51, v120, v121
	v_max3_f32 v50, v50, v119, v90
	v_max3_f32 v51, v51, v92, v93
	v_max3_f32 v50, v50, v91, v122
	v_max3_f32 v51, v51, v124, v125
	v_max3_f32 v50, v50, v123, v94
	v_max3_f32 v51, v51, v96, v97
	v_max3_f32 v50, v50, v95, v51
	v_mov_b32_e32 v51, v50
	s_nop 1
	v_permlane32_swap_b32_e32 v50, v51
	v_max_f32_e32 v50, v50, v51
	s_mov_b32 s6, 0x41000000
	v_cmp_lt_f32_e32 vcc, s6, v50
	s_cmp_lg_u64 vcc, 0
	v_add_f32_e32 v67, v206, v54
	s_cselect_b64 s[6:7], -1, 0
	s_cbranch_vccnz .LBB1_86
	s_mov_b64 s[8:9], -1
	v_mov_b32_e32 v66, v35

.LBB1_38:
	ds_read_b64_tr_b16 v[186:187], v216 offset:40960
	ds_read_b64_tr_b16 v[188:189], v216 offset:41472
	s_waitcnt lgkmcnt(9)
	v_mfma_f32_32x32x16_f16 v[110:125], v[86:89], v[174:177], v[50:65]
	v_add_f32_e32 v82, v94, v95
	v_add_f32_e32 v82, v96, v82
	v_add_f32_e32 v82, v97, v82
	v_add_f32_e32 v82, v98, v82
	v_add_f32_e32 v82, v99, v82
	v_cvt_pkrtz_f16_f32 v158, v94, v95
	v_cvt_pkrtz_f16_f32 v159, v96, v97
	ds_read_b64_tr_b16 v[182:183], v216 offset:45056
	ds_read_b64_tr_b16 v[184:185], v216 offset:45568
	v_add_f32_e32 v82, v100, v82
	v_add_f32_e32 v82, v101, v82
	v_add_f32_e32 v82, v102, v82
	v_add_f32_e32 v126, v103, v82
	s_waitcnt lgkmcnt(10)
	v_mfma_f32_32x32x16_f16 v[82:97], v[194:197], v[174:177], v[50:65]
	v_cvt_pkrtz_f16_f32 v160, v98, v99
	v_cvt_pkrtz_f16_f32 v161, v100, v101
	ds_read_b64_tr_b16 v[178:179], v216 offset:41984
	ds_read_b64_tr_b16 v[180:181], v216 offset:42496
	s_waitcnt lgkmcnt(11)
	v_mfma_f32_32x32x16_f16 v[110:125], v[198:201], v[170:173], v[110:125]
	v_add_f32_e32 v98, v104, v126
	v_add_f32_e32 v98, v105, v98
	v_add_f32_e32 v98, v106, v98
	v_add_f32_e32 v98, v107, v98
	v_cvt_pkrtz_f16_f32 v154, v102, v103
	v_cvt_pkrtz_f16_f32 v155, v104, v105
	ds_read_b64_tr_b16 v[142:143], v216 offset:46080
	ds_read_b64_tr_b16 v[144:145], v216 offset:46592
	s_waitcnt lgkmcnt(12)
	v_mfma_f32_32x32x16_f16 v[82:97], v[46:49], v[170:173], v[82:97]
	v_add_f32_e32 v98, v108, v98
	v_add_f32_e32 v98, v109, v98
	v_add_f32_e32 v98, v66, v98
	v_add_f32_e32 v98, v67, v98
	v_cvt_pkrtz_f16_f32 v156, v106, v107
	v_cvt_pkrtz_f16_f32 v157, v108, v109
	ds_read_b64_tr_b16 v[138:139], v216 offset:43008
	ds_read_b64_tr_b16 v[140:141], v216 offset:43520
	s_waitcnt lgkmcnt(13)
	v_mfma_f32_32x32x16_f16 v[110:125], v[190:193], v[166:169], v[110:125]
	v_add_f32_e32 v46, v68, v98
	v_add_f32_e32 v46, v69, v46
	v_add_f32_e32 v46, v70, v46
	v_add_f32_e32 v46, v71, v46
	v_cvt_pkrtz_f16_f32 v150, v66, v67
	v_cvt_pkrtz_f16_f32 v151, v68, v69
	ds_read_b64_tr_b16 v[134:135], v216 offset:47104
	ds_read_b64_tr_b16 v[136:137], v216 offset:47616
	s_waitcnt lgkmcnt(14)
	v_mfma_f32_32x32x16_f16 v[82:97], v[38:41], v[166:169], v[82:97]
	v_add_f32_e32 v46, v72, v46
	v_add_f32_e32 v46, v73, v46
	v_add_f32_e32 v46, v74, v46
	v_add_f32_e32 v46, v75, v46
	v_cvt_pkrtz_f16_f32 v152, v70, v71
	v_cvt_pkrtz_f16_f32 v153, v72, v73
	ds_read_b64_tr_b16 v[130:131], v216 offset:44032
	ds_read_b64_tr_b16 v[132:133], v216 offset:44544
	s_waitcnt lgkmcnt(14)
	v_mfma_f32_32x32x16_f16 v[110:125], v[42:45], v[162:165], v[110:125]
	v_add_f32_e32 v38, v76, v46
	v_add_f32_e32 v38, v77, v38
	v_add_f32_e32 v38, v78, v38
	v_add_f32_e32 v38, v79, v38
	v_cvt_pkrtz_f16_f32 v146, v74, v75
	v_cvt_pkrtz_f16_f32 v147, v76, v77
	ds_read_b64_tr_b16 v[126:127], v216 offset:48128
	ds_read_b64_tr_b16 v[128:129], v216 offset:48640
	v_mfma_f32_32x32x16_f16 v[82:97], v[34:37], v[162:165], v[82:97]
	v_add_f32_e32 v38, v80, v38
	v_add_f32_e32 v38, v81, v38
	v_add_f32_e32 v38, 0, v38
	v_cvt_pkrtz_f16_f32 v148, v78, v79
	v_cvt_pkrtz_f16_f32 v149, v80, v81
	v_max_f32_e32 v34, v111, v111
	v_max_f32_e32 v35, v110, v110
	v_max_f32_e32 v34, v35, v34
	s_nop 3
	v_max3_f32 v35, v112, v113, v83
	v_max3_f32 v34, v34, v82, v84
	v_max3_f32 v34, v34, v85, v114
	v_max3_f32 v35, v35, v116, v117
	v_max3_f32 v34, v34, v115, v86
	v_max3_f32 v35, v35, v88, v89
	v_max3_f32 v34, v34, v87, v118
	v_max3_f32 v35, v35, v120, v121
	v_max3_f32 v34, v34, v119, v90
	v_max3_f32 v35, v35, v92, v93
	v_max3_f32 v34, v34, v91, v122
	v_max3_f32 v35, v35, v124, v125
	v_max3_f32 v34, v34, v123, v94
	v_max3_f32 v35, v35, v96, v97
	v_max3_f32 v34, v34, v95, v35
	v_mov_b32_e32 v35, v34
	s_nop 1
	v_permlane32_swap_b32_e32 v34, v35
	v_max_f32_e32 v34, v34, v35
	s_mov_b32 s6, 0x41000000
	v_cmp_lt_f32_e32 vcc, s6, v34
	s_cmp_lg_u64 vcc, 0
	v_add_f32_e32 v79, v207, v38
	s_cselect_b64 s[6:7], -1, 0
	s_cbranch_vccnz .LBB1_89
	s_mov_b64 s[8:9], -1
	v_mov_b32_e32 v78, v51

.LBB1_44:
	ds_read_b64_tr_b16 v[182:183], v216 offset:24576
	ds_read_b64_tr_b16 v[184:185], v216 offset:25088
	s_waitcnt lgkmcnt(9)
	v_mfma_f32_32x32x16_f16 v[110:125], v[78:81], v[174:177], v[34:49]
	v_add_f32_e32 v82, v94, v95
	v_add_f32_e32 v82, v96, v82
	v_add_f32_e32 v82, v97, v82
	v_add_f32_e32 v82, v98, v82
	v_add_f32_e32 v82, v99, v82
	v_cvt_pkrtz_f16_f32 v158, v94, v95
	v_cvt_pkrtz_f16_f32 v159, v96, v97
	ds_read_b64_tr_b16 v[178:179], v216 offset:28672
	ds_read_b64_tr_b16 v[180:181], v216 offset:29184
	v_add_f32_e32 v78, v100, v82
	v_add_f32_e32 v78, v101, v78
	v_add_f32_e32 v78, v102, v78
	v_add_f32_e32 v94, v103, v78
	s_waitcnt lgkmcnt(10)
	v_mfma_f32_32x32x16_f16 v[78:93], v[194:197], v[174:177], v[34:49]
	v_cvt_pkrtz_f16_f32 v160, v98, v99
	v_cvt_pkrtz_f16_f32 v161, v100, v101
	ds_read_b64_tr_b16 v[174:175], v216 offset:25600
	ds_read_b64_tr_b16 v[176:177], v216 offset:26112
	s_waitcnt lgkmcnt(11)
	v_mfma_f32_32x32x16_f16 v[110:125], v[198:201], v[170:173], v[110:125]
	v_add_f32_e32 v94, v104, v94
	v_add_f32_e32 v94, v105, v94
	v_add_f32_e32 v94, v106, v94
	v_add_f32_e32 v94, v107, v94
	v_cvt_pkrtz_f16_f32 v154, v102, v103
	v_cvt_pkrtz_f16_f32 v155, v104, v105
	ds_read_b64_tr_b16 v[142:143], v216 offset:29696
	ds_read_b64_tr_b16 v[144:145], v216 offset:30208
	s_waitcnt lgkmcnt(12)
	v_mfma_f32_32x32x16_f16 v[78:93], v[186:189], v[170:173], v[78:93]
	v_add_f32_e32 v94, v108, v94
	v_add_f32_e32 v94, v109, v94
	v_add_f32_e32 v94, v62, v94
	v_add_f32_e32 v94, v63, v94
	v_cvt_pkrtz_f16_f32 v156, v106, v107
	v_cvt_pkrtz_f16_f32 v157, v108, v109
	ds_read_b64_tr_b16 v[138:139], v216 offset:26624
	ds_read_b64_tr_b16 v[140:141], v216 offset:27136
	s_waitcnt lgkmcnt(13)
	v_mfma_f32_32x32x16_f16 v[110:125], v[190:193], v[166:169], v[110:125]
	v_add_f32_e32 v94, v64, v94
	v_add_f32_e32 v94, v65, v94
	v_add_f32_e32 v94, v66, v94
	v_add_f32_e32 v94, v67, v94
	v_cvt_pkrtz_f16_f32 v150, v62, v63
	v_cvt_pkrtz_f16_f32 v151, v64, v65
	ds_read_b64_tr_b16 v[134:135], v216 offset:30720
	ds_read_b64_tr_b16 v[136:137], v216 offset:31232
	s_waitcnt lgkmcnt(14)
	v_mfma_f32_32x32x16_f16 v[78:93], v[54:57], v[166:169], v[78:93]
	v_add_f32_e32 v62, v68, v94
	v_add_f32_e32 v62, v69, v62
	v_add_f32_e32 v62, v70, v62
	v_add_f32_e32 v62, v71, v62
	v_cvt_pkrtz_f16_f32 v152, v66, v67
	v_cvt_pkrtz_f16_f32 v153, v68, v69
	ds_read_b64_tr_b16 v[130:131], v216 offset:27648
	ds_read_b64_tr_b16 v[132:133], v216 offset:28160
	s_waitcnt lgkmcnt(14)
	v_mfma_f32_32x32x16_f16 v[110:125], v[58:61], v[162:165], v[110:125]
	v_add_f32_e32 v54, v72, v62
	v_add_f32_e32 v54, v73, v54
	v_add_f32_e32 v54, v74, v54
	v_add_f32_e32 v54, v75, v54
	v_cvt_pkrtz_f16_f32 v146, v70, v71
	v_cvt_pkrtz_f16_f32 v147, v72, v73
	ds_read_b64_tr_b16 v[126:127], v216 offset:31744
	ds_read_b64_tr_b16 v[128:129], v216 offset:32256
	v_mfma_f32_32x32x16_f16 v[78:93], v[50:53], v[162:165], v[78:93]
	v_add_f32_e32 v54, v76, v54
	v_add_f32_e32 v54, v77, v54
	v_add_f32_e32 v54, 0, v54
	v_cvt_pkrtz_f16_f32 v148, v74, v75
	v_cvt_pkrtz_f16_f32 v149, v76, v77
	v_max_f32_e32 v50, v111, v111
	v_max_f32_e32 v51, v110, v110
	v_max_f32_e32 v50, v51, v50
	s_nop 3
	v_max3_f32 v51, v112, v113, v79
	v_max3_f32 v50, v50, v78, v80
	v_max3_f32 v50, v50, v81, v114
	v_max3_f32 v51, v51, v116, v117
	v_max3_f32 v50, v50, v115, v82
	v_max3_f32 v51, v51, v84, v85
	v_max3_f32 v50, v50, v83, v118
	v_max3_f32 v51, v51, v120, v121
	v_max3_f32 v50, v50, v119, v86
	v_max3_f32 v51, v51, v88, v89
	v_max3_f32 v50, v50, v87, v122
	v_max3_f32 v51, v51, v124, v125
	v_max3_f32 v50, v50, v123, v90
	v_max3_f32 v51, v51, v92, v93
	v_max3_f32 v50, v50, v91, v51
	v_mov_b32_e32 v51, v50
	s_nop 1
	v_permlane32_swap_b32_e32 v50, v51
	v_max_f32_e32 v50, v50, v51
	s_mov_b32 s6, 0x41000000
	v_cmp_lt_f32_e32 vcc, s6, v50
	s_cmp_lg_u64 vcc, 0
	v_add_f32_e32 v63, v207, v54
	s_cselect_b64 s[6:7], -1, 0
	s_cbranch_vccnz .LBB1_92
	s_mov_b64 s[8:9], -1
	v_mov_b32_e32 v62, v35
